# PEER gather u-pass: bf16 dot chains use v_dot2_f32_bf16 with a constant-0 first addend; 32 accumulator zero moves per token-slice removed; on top of v062
# speedup vs baseline: 1.0021x; 1.0021x over previous
.LBB0_746:
	ds_read_b128 v[2:5], v123
	ds_read_b128 v[82:85], v123 offset:128
	s_waitcnt lgkmcnt(0)
	v_and_b32_e32 v6, 0xffff, v2
	v_lshrrev_b32_e32 v2, 16, v2
	v_mad_u32_u24 v6, v6, s30, v110
	v_mad_u32_u24 v2, v2, s30, v110
	global_load_dwordx2 v[10:11], v6, s[26:27] offset:16
	s_nop 0
	global_load_dwordx4 v[6:9], v6, s[26:27]
	s_nop 0
	global_load_dwordx2 v[16:17], v2, s[26:27] offset:16
	global_load_dwordx4 v[12:15], v2, s[26:27]
	v_and_b32_e32 v2, 0xffff, v3
	v_mad_u32_u24 v2, v2, s30, v110
	global_load_dwordx2 v[130:131], v2, s[26:27] offset:16
	global_load_dwordx4 v[126:129], v2, s[26:27]
	v_lshrrev_b32_e32 v2, 16, v3
	v_mad_u32_u24 v2, v2, s30, v110
	global_load_dwordx2 v[136:137], v2, s[26:27] offset:16
	global_load_dwordx4 v[132:135], v2, s[26:27]
	v_and_b32_e32 v2, 0xffff, v4
	v_mad_u32_u24 v2, v2, s30, v110
	global_load_dwordx2 v[142:143], v2, s[26:27] offset:16
	global_load_dwordx4 v[138:141], v2, s[26:27]
	v_lshrrev_b32_e32 v3, 16, v4
	v_and_b32_e32 v2, 0xffff, v5
	v_lshrrev_b32_e32 v4, 16, v5
	v_mad_u32_u24 v3, v3, s30, v110
	v_mad_u32_u24 v2, v2, s30, v110
	v_mad_u32_u24 v4, v4, s30, v110
	global_load_dwordx2 v[148:149], v3, s[26:27] offset:16
	global_load_dwordx4 v[144:147], v3, s[26:27]
	global_load_dwordx2 v[154:155], v2, s[26:27] offset:16
	global_load_dwordx4 v[150:153], v2, s[26:27]
	global_load_dwordx2 v[160:161], v4, s[26:27] offset:16
	global_load_dwordx4 v[156:159], v4, s[26:27]
	s_and_b64 vcc, exec, s[12:13]
	s_waitcnt vmcnt(14)
	v_cvt_scalef32_pk32_bf16_fp6 v[50:65], v[6:11], 1.0
	v_dot2_f32_bf16 v106, v50, v78, 0
	s_waitcnt vmcnt(12)
	v_cvt_scalef32_pk32_bf16_fp6 v[34:49], v[12:17], 1.0
	v_dot2_f32_bf16 v102, v34, v78, 0
	v_dot2_f32_bf16 v104, v35, v79, 0
	s_waitcnt vmcnt(10)
	v_cvt_scalef32_pk32_bf16_fp6 v[18:33], v[126:131], 1.0
	v_dot2_f32_bf16 v98, v18, v78, 0
	v_dot2_f32_bf16 v98, v20, v80, v98
	s_waitcnt vmcnt(8)
	v_cvt_scalef32_pk32_bf16_fp6 v[2:17], v[132:137], 1.0
	v_dot2_f32_bf16 v94, v2, v78, 0
	v_dot2_f32_bf16 v96, v3, v79, 0
	v_dot2_f32_bf16 v94, v4, v80, v94
	v_dot2_f32_bf16 v96, v5, v81, v96
	v_dot2_f32_bf16 v94, v6, v74, v94
	v_dot2_f32_bf16 v96, v7, v75, v96
	v_dot2_f32_bf16 v94, v8, v76, v94
	v_dot2_f32_bf16 v96, v9, v77, v96
	v_dot2_f32_bf16 v94, v10, v70, v94
	v_dot2_f32_bf16 v96, v11, v71, v96
	v_dot2_f32_bf16 v94, v12, v72, v94
	v_dot2_f32_bf16 v96, v13, v73, v96
	v_dot2_f32_bf16 v94, v14, v66, v94
	v_dot2_f32_bf16 v96, v15, v67, v96
	v_dot2_f32_bf16 v94, v16, v68, v94
	v_dot2_f32_bf16 v96, v17, v69, v96
	s_waitcnt vmcnt(6)
	v_cvt_scalef32_pk32_bf16_fp6 v[2:17], v[138:143], 1.0
	v_dot2_f32_bf16 v18, v2, v78, 0
	v_dot2_f32_bf16 v20, v3, v79, 0
	v_dot2_f32_bf16 v18, v4, v80, v18
	v_dot2_f32_bf16 v20, v5, v81, v20
	v_dot2_f32_bf16 v18, v6, v74, v18
	v_dot2_f32_bf16 v20, v7, v75, v20
	v_dot2_f32_bf16 v18, v8, v76, v18
	v_dot2_f32_bf16 v20, v9, v77, v20
	v_dot2_f32_bf16 v18, v10, v70, v18
	v_dot2_f32_bf16 v20, v11, v71, v20
	v_dot2_f32_bf16 v18, v12, v72, v18
	v_dot2_f32_bf16 v20, v13, v73, v20
	v_dot2_f32_bf16 v18, v14, v66, v18
	v_dot2_f32_bf16 v20, v15, v67, v20
	v_dot2_f32_bf16 v98, v22, v74, v98
	v_dot2_f32_bf16 v18, v16, v68, v18
	v_dot2_f32_bf16 v20, v17, v69, v20
	s_waitcnt vmcnt(4)
	v_cvt_scalef32_pk32_bf16_fp6 v[2:17], v[144:149], 1.0
	v_dot2_f32_bf16 v22, v2, v78, 0
	v_and_b32_e32 v2, 0xffff, v82
	v_dot2_f32_bf16 v102, v36, v80, v102
	v_dot2_f32_bf16 v104, v37, v81, v104
	v_mad_u32_u24 v2, v2, s30, v110
	v_dot2_f32_bf16 v102, v38, v74, v102
	v_dot2_f32_bf16 v104, v39, v75, v104
	global_load_dwordx2 v[38:39], v2, s[26:27] offset:16
	global_load_dwordx4 v[34:37], v2, s[26:27]
	v_dot2_f32_bf16 v98, v24, v76, v98
	v_dot2_f32_bf16 v100, v19, v79, 0
	v_dot2_f32_bf16 v102, v40, v76, v102
	v_dot2_f32_bf16 v104, v41, v77, v104
	v_dot2_f32_bf16 v24, v3, v79, 0
	v_lshrrev_b32_e32 v19, 16, v82
	v_dot2_f32_bf16 v102, v42, v70, v102
	v_dot2_f32_bf16 v104, v43, v71, v104
	v_dot2_f32_bf16 v22, v4, v80, v22
	v_dot2_f32_bf16 v24, v5, v81, v24
	v_mad_u32_u24 v19, v19, s30, v110
	v_dot2_f32_bf16 v102, v44, v72, v102
	v_dot2_f32_bf16 v104, v45, v73, v104
	v_dot2_f32_bf16 v22, v6, v74, v22
	v_dot2_f32_bf16 v24, v7, v75, v24
	global_load_dwordx2 v[44:45], v19, s[26:27] offset:16
	global_load_dwordx4 v[40:43], v19, s[26:27]
	v_dot2_f32_bf16 v22, v8, v76, v22
	v_dot2_f32_bf16 v24, v9, v77, v24
	v_dot2_f32_bf16 v22, v10, v70, v22
	v_dot2_f32_bf16 v24, v11, v71, v24
	v_dot2_f32_bf16 v22, v12, v72, v22
	v_dot2_f32_bf16 v24, v13, v73, v24
	v_dot2_f32_bf16 v98, v26, v70, v98
	v_dot2_f32_bf16 v22, v14, v66, v22
	v_dot2_f32_bf16 v24, v15, v67, v24
	v_dot2_f32_bf16 v98, v28, v72, v98
	v_dot2_f32_bf16 v22, v16, v68, v22
	v_dot2_f32_bf16 v24, v17, v69, v24
	s_waitcnt vmcnt(6)
	v_cvt_scalef32_pk32_bf16_fp6 v[2:17], v[150:155], 1.0
	v_dot2_f32_bf16 v26, v2, v78, 0
	v_dot2_f32_bf16 v28, v3, v79, 0
	v_and_b32_e32 v2, 0xffff, v83
	v_dot2_f32_bf16 v102, v46, v66, v102
	v_dot2_f32_bf16 v104, v47, v67, v104
	v_dot2_f32_bf16 v26, v4, v80, v26
	v_dot2_f32_bf16 v28, v5, v81, v28
	v_mad_u32_u24 v2, v2, s30, v110
	v_dot2_f32_bf16 v108, v51, v79, 0
	v_dot2_f32_bf16 v102, v48, v68, v102
	v_dot2_f32_bf16 v104, v49, v69, v104
	v_dot2_f32_bf16 v26, v6, v74, v26
	v_dot2_f32_bf16 v28, v7, v75, v28
	global_load_dwordx2 v[50:51], v2, s[26:27] offset:16
	global_load_dwordx4 v[46:49], v2, s[26:27]
	v_dot2_f32_bf16 v26, v8, v76, v26
	v_dot2_f32_bf16 v28, v9, v77, v28
	v_dot2_f32_bf16 v26, v10, v70, v26
	v_dot2_f32_bf16 v28, v11, v71, v28
	v_dot2_f32_bf16 v26, v12, v72, v26
	v_dot2_f32_bf16 v28, v13, v73, v28
	v_dot2_f32_bf16 v26, v14, v66, v26
	v_dot2_f32_bf16 v28, v15, v67, v28
	v_dot2_f32_bf16 v98, v30, v66, v98
	v_dot2_f32_bf16 v26, v16, v68, v26
	v_dot2_f32_bf16 v28, v17, v69, v28
	s_waitcnt vmcnt(6)
	v_cvt_scalef32_pk32_bf16_fp6 v[2:17], v[156:161], 1.0
	v_dot2_f32_bf16 v106, v52, v80, v106
	v_dot2_f32_bf16 v108, v53, v81, v108
	v_dot2_f32_bf16 v30, v2, v78, 0
	v_lshrrev_b32_e32 v2, 16, v83
	v_dot2_f32_bf16 v106, v54, v74, v106
	v_dot2_f32_bf16 v108, v55, v75, v108
	v_mad_u32_u24 v2, v2, s30, v110
	v_dot2_f32_bf16 v106, v56, v76, v106
	v_dot2_f32_bf16 v108, v57, v77, v108
	global_load_dwordx2 v[56:57], v2, s[26:27] offset:16
	global_load_dwordx4 v[52:55], v2, s[26:27]
	v_dot2_f32_bf16 v106, v58, v70, v106
	v_dot2_f32_bf16 v108, v59, v71, v108
	v_and_b32_e32 v2, 0xffff, v84
	v_dot2_f32_bf16 v106, v60, v72, v106
	v_dot2_f32_bf16 v108, v61, v73, v108
	v_mad_u32_u24 v2, v2, s30, v110
	v_dot2_f32_bf16 v106, v62, v66, v106
	v_dot2_f32_bf16 v108, v63, v67, v108
	global_load_dwordx2 v[62:63], v2, s[26:27] offset:16
	global_load_dwordx4 v[58:61], v2, s[26:27]
	v_lshrrev_b32_e32 v2, 16, v84
	v_mad_u32_u24 v2, v2, s30, v110
	global_load_dwordx2 v[130:131], v2, s[26:27] offset:16
	global_load_dwordx4 v[126:129], v2, s[26:27]
	v_and_b32_e32 v2, 0xffff, v85
	v_mad_u32_u24 v2, v2, s30, v110
	global_load_dwordx2 v[136:137], v2, s[26:27] offset:16
	global_load_dwordx4 v[132:135], v2, s[26:27]
	v_lshrrev_b32_e32 v2, 16, v85
	v_mad_u32_u24 v2, v2, s30, v110
	global_load_dwordx2 v[142:143], v2, s[26:27] offset:16
	global_load_dwordx4 v[138:141], v2, s[26:27]
	v_dot2_f32_bf16 v98, v32, v68, v98
	v_dot2_f32_bf16 v32, v3, v79, 0
	v_dot2_f32_bf16 v30, v4, v80, v30
	v_dot2_f32_bf16 v32, v5, v81, v32
	v_dot2_f32_bf16 v30, v6, v74, v30
	v_dot2_f32_bf16 v32, v7, v75, v32
	v_dot2_f32_bf16 v30, v8, v76, v30
	v_dot2_f32_bf16 v32, v9, v77, v32
	v_dot2_f32_bf16 v30, v10, v70, v30
	v_dot2_f32_bf16 v32, v11, v71, v32
	v_dot2_f32_bf16 v30, v12, v72, v30
	v_dot2_f32_bf16 v32, v13, v73, v32
	v_dot2_f32_bf16 v30, v14, v66, v30
	v_dot2_f32_bf16 v32, v15, v67, v32
	v_dot2_f32_bf16 v30, v16, v68, v30
	v_dot2_f32_bf16 v32, v17, v69, v32
	s_waitcnt vmcnt(14)
	v_cvt_scalef32_pk32_bf16_fp6 v[2:17], v[34:39], 1.0
	v_dot2_f32_bf16 v107, v2, v78, 0
	v_dot2_f32_bf16 v109, v3, v79, 0
	v_dot2_f32_bf16 v107, v4, v80, v107
	v_dot2_f32_bf16 v109, v5, v81, v109
	v_dot2_f32_bf16 v107, v6, v74, v107
	v_dot2_f32_bf16 v109, v7, v75, v109
	v_dot2_f32_bf16 v107, v8, v76, v107
	v_dot2_f32_bf16 v109, v9, v77, v109
	v_dot2_f32_bf16 v107, v10, v70, v107
	v_dot2_f32_bf16 v109, v11, v71, v109
	v_dot2_f32_bf16 v107, v12, v72, v107
	v_dot2_f32_bf16 v109, v13, v73, v109
	v_dot2_f32_bf16 v107, v14, v66, v107
	v_dot2_f32_bf16 v109, v15, v67, v109
	v_dot2_f32_bf16 v107, v16, v68, v107
	v_dot2_f32_bf16 v109, v17, v69, v109
	s_waitcnt vmcnt(12)
	v_cvt_scalef32_pk32_bf16_fp6 v[2:17], v[40:45], 1.0
	v_dot2_f32_bf16 v103, v2, v78, 0
	v_dot2_f32_bf16 v105, v3, v79, 0
	v_dot2_f32_bf16 v103, v4, v80, v103
	v_dot2_f32_bf16 v105, v5, v81, v105
	v_dot2_f32_bf16 v103, v6, v74, v103
	v_dot2_f32_bf16 v105, v7, v75, v105
	v_dot2_f32_bf16 v103, v8, v76, v103
	v_dot2_f32_bf16 v105, v9, v77, v105
	v_dot2_f32_bf16 v103, v10, v70, v103
	v_dot2_f32_bf16 v105, v11, v71, v105
	v_dot2_f32_bf16 v103, v12, v72, v103
	v_dot2_f32_bf16 v105, v13, v73, v105
	v_dot2_f32_bf16 v103, v14, v66, v103
	v_dot2_f32_bf16 v105, v15, v67, v105
	v_dot2_f32_bf16 v103, v16, v68, v103
	v_dot2_f32_bf16 v105, v17, v69, v105
	s_waitcnt vmcnt(10)
	v_cvt_scalef32_pk32_bf16_fp6 v[2:17], v[46:51], 1.0
	v_dot2_f32_bf16 v99, v2, v78, 0
	v_dot2_f32_bf16 v101, v3, v79, 0
	v_dot2_f32_bf16 v99, v4, v80, v99
	v_dot2_f32_bf16 v101, v5, v81, v101
	v_dot2_f32_bf16 v99, v6, v74, v99
	v_dot2_f32_bf16 v101, v7, v75, v101
	v_dot2_f32_bf16 v99, v8, v76, v99
	v_dot2_f32_bf16 v101, v9, v77, v101
	v_dot2_f32_bf16 v99, v10, v70, v99
	v_dot2_f32_bf16 v101, v11, v71, v101
	v_dot2_f32_bf16 v99, v12, v72, v99
	v_dot2_f32_bf16 v101, v13, v73, v101
	v_dot2_f32_bf16 v99, v14, v66, v99
	v_dot2_f32_bf16 v101, v15, v67, v101
	v_dot2_f32_bf16 v99, v16, v68, v99
	v_dot2_f32_bf16 v101, v17, v69, v101
	s_waitcnt vmcnt(8)
	v_cvt_scalef32_pk32_bf16_fp6 v[2:17], v[52:57], 1.0
	v_dot2_f32_bf16 v95, v2, v78, 0
	v_dot2_f32_bf16 v97, v3, v79, 0
	v_dot2_f32_bf16 v95, v4, v80, v95
	v_dot2_f32_bf16 v97, v5, v81, v97
	v_dot2_f32_bf16 v95, v6, v74, v95
	v_dot2_f32_bf16 v97, v7, v75, v97
	v_dot2_f32_bf16 v95, v8, v76, v95
	v_dot2_f32_bf16 v97, v9, v77, v97
	v_dot2_f32_bf16 v95, v10, v70, v95
	v_dot2_f32_bf16 v97, v11, v71, v97
	v_dot2_f32_bf16 v95, v12, v72, v95
	v_dot2_f32_bf16 v97, v13, v73, v97
	v_dot2_f32_bf16 v95, v14, v66, v95
	v_dot2_f32_bf16 v97, v15, v67, v97
	v_dot2_f32_bf16 v100, v21, v81, v100
	v_dot2_f32_bf16 v95, v16, v68, v95
	v_dot2_f32_bf16 v97, v17, v69, v97
	s_waitcnt vmcnt(6)
	v_cvt_scalef32_pk32_bf16_fp6 v[2:17], v[58:63], 1.0
	v_dot2_f32_bf16 v19, v2, v78, 0
	v_dot2_f32_bf16 v21, v3, v79, 0
	v_dot2_f32_bf16 v19, v4, v80, v19
	v_dot2_f32_bf16 v21, v5, v81, v21
	v_dot2_f32_bf16 v19, v6, v74, v19
	v_dot2_f32_bf16 v21, v7, v75, v21
	v_dot2_f32_bf16 v19, v8, v76, v19
	v_dot2_f32_bf16 v21, v9, v77, v21
	v_dot2_f32_bf16 v19, v10, v70, v19
	v_dot2_f32_bf16 v21, v11, v71, v21
	v_dot2_f32_bf16 v19, v12, v72, v19
	v_dot2_f32_bf16 v21, v13, v73, v21
	v_dot2_f32_bf16 v100, v23, v75, v100
	v_dot2_f32_bf16 v19, v14, v66, v19
	v_dot2_f32_bf16 v21, v15, v67, v21
	v_dot2_f32_bf16 v100, v25, v77, v100
	v_dot2_f32_bf16 v19, v16, v68, v19
	v_dot2_f32_bf16 v21, v17, v69, v21
	s_waitcnt vmcnt(4)
	v_cvt_scalef32_pk32_bf16_fp6 v[2:17], v[126:131], 1.0
	v_dot2_f32_bf16 v23, v2, v78, 0
	v_dot2_f32_bf16 v25, v3, v79, 0
	v_dot2_f32_bf16 v23, v4, v80, v23
	v_dot2_f32_bf16 v25, v5, v81, v25
	v_dot2_f32_bf16 v23, v6, v74, v23
	v_dot2_f32_bf16 v25, v7, v75, v25
	v_dot2_f32_bf16 v23, v8, v76, v23
	v_dot2_f32_bf16 v25, v9, v77, v25
	v_dot2_f32_bf16 v23, v10, v70, v23
	v_dot2_f32_bf16 v25, v11, v71, v25
	v_dot2_f32_bf16 v23, v12, v72, v23
	v_dot2_f32_bf16 v25, v13, v73, v25
	v_dot2_f32_bf16 v100, v27, v71, v100
	v_dot2_f32_bf16 v23, v14, v66, v23
	v_dot2_f32_bf16 v25, v15, v67, v25
	v_dot2_f32_bf16 v100, v29, v73, v100
	v_dot2_f32_bf16 v23, v16, v68, v23
	v_dot2_f32_bf16 v25, v17, v69, v25
	s_waitcnt vmcnt(2)
	v_cvt_scalef32_pk32_bf16_fp6 v[2:17], v[132:137], 1.0
	v_dot2_f32_bf16 v27, v2, v78, 0
	v_dot2_f32_bf16 v29, v3, v79, 0
	v_dot2_f32_bf16 v27, v4, v80, v27
	v_dot2_f32_bf16 v29, v5, v81, v29
	v_dot2_f32_bf16 v27, v6, v74, v27
	v_dot2_f32_bf16 v29, v7, v75, v29
	v_dot2_f32_bf16 v27, v8, v76, v27
	v_dot2_f32_bf16 v29, v9, v77, v29
	v_dot2_f32_bf16 v27, v10, v70, v27
	v_dot2_f32_bf16 v29, v11, v71, v29
	v_dot2_f32_bf16 v27, v12, v72, v27
	v_dot2_f32_bf16 v29, v13, v73, v29
	v_dot2_f32_bf16 v100, v31, v67, v100
	v_dot2_f32_bf16 v27, v14, v66, v27
	v_dot2_f32_bf16 v29, v15, v67, v29
	v_dot2_f32_bf16 v100, v33, v69, v100
	v_dot2_f32_bf16 v27, v16, v68, v27
	v_dot2_f32_bf16 v29, v17, v69, v29
	s_waitcnt vmcnt(0)
	v_cvt_scalef32_pk32_bf16_fp6 v[2:17], v[138:143], 1.0
	v_dot2_f32_bf16 v31, v2, v78, 0
	v_dot2_f32_bf16 v33, v3, v79, 0
	v_dot2_f32_bf16 v31, v4, v80, v31
	v_dot2_f32_bf16 v33, v5, v81, v33
	v_dot2_f32_bf16 v31, v6, v74, v31
	v_dot2_f32_bf16 v33, v7, v75, v33
	v_dot2_f32_bf16 v31, v8, v76, v31
	v_dot2_f32_bf16 v33, v9, v77, v33
	v_dot2_f32_bf16 v31, v10, v70, v31
	v_dot2_f32_bf16 v33, v11, v71, v33
	v_dot2_f32_bf16 v31, v12, v72, v31
	v_dot2_f32_bf16 v33, v13, v73, v33
	v_dot2_f32_bf16 v31, v14, v66, v31
	v_dot2_f32_bf16 v33, v15, v67, v33
	v_pk_add_f32 v[8:9], v[104:105], v[102:103]
	v_pk_add_f32 v[10:11], v[24:25], v[22:23]
	v_dot2_f32_bf16 v31, v16, v68, v31
	v_dot2_f32_bf16 v33, v17, v69, v33
	v_cndmask_b32_e64 v7, v8, v10, s[4:5]
	v_pk_add_f32 v[14:15], v[100:101], v[98:99]
	v_pk_add_f32 v[16:17], v[28:29], v[26:27]
	v_dot2_f32_bf16 v106, v64, v68, v106
	v_dot2_f32_bf16 v108, v65, v69, v108
	v_pk_add_f32 v[4:5], v[20:21], v[18:19]
	ds_bpermute_b32 v12, v119, v7
	v_cndmask_b32_e64 v7, v14, v16, s[4:5]
	v_pk_add_f32 v[20:21], v[96:97], v[94:95]
	v_pk_add_f32 v[22:23], v[32:33], v[30:31]
	v_pk_add_f32 v[2:3], v[108:109], v[106:107]
	ds_bpermute_b32 v18, v119, v7
	v_cndmask_b32_e64 v7, v20, v22, s[4:5]
	v_cndmask_b32_e64 v6, v2, v4, s[4:5]
	ds_bpermute_b32 v24, v119, v7
	v_cndmask_b32_e64 v7, v3, v5, s[4:5]
	ds_bpermute_b32 v6, v119, v6
	ds_bpermute_b32 v7, v119, v7
	v_cndmask_b32_e64 v3, v5, v3, s[4:5]
	v_cndmask_b32_e64 v2, v4, v2, s[4:5]
	v_cndmask_b32_e64 v5, v15, v17, s[4:5]
	ds_bpermute_b32 v19, v119, v5
	s_waitcnt lgkmcnt(1)
	v_pk_add_f32 v[2:3], v[2:3], v[6:7]
	v_cndmask_b32_e64 v7, v9, v11, s[4:5]
	ds_bpermute_b32 v13, v119, v7
	v_cndmask_b32_e64 v7, v21, v23, s[4:5]
	ds_bpermute_b32 v25, v119, v7
	v_cndmask_b32_e64 v9, v11, v9, s[4:5]
	v_cndmask_b32_e64 v8, v10, v8, s[4:5]
	v_cndmask_b32_e64 v11, v23, v21, s[4:5]
	v_cndmask_b32_e64 v10, v22, v20, s[4:5]
	v_cndmask_b32_e64 v5, v17, v15, s[4:5]
	v_cndmask_b32_e64 v4, v16, v14, s[4:5]
	s_waitcnt lgkmcnt(1)
	v_pk_add_f32 v[8:9], v[8:9], v[12:13]
	s_waitcnt lgkmcnt(0)
	v_pk_add_f32 v[10:11], v[10:11], v[24:25]
	v_pk_add_f32 v[4:5], v[4:5], v[18:19]
	v_cndmask_b32_e64 v7, v8, v10, s[6:7]
	v_cndmask_b32_e64 v6, v2, v4, s[6:7]
	ds_bpermute_b32 v12, v120, v7
	v_cndmask_b32_e64 v7, v3, v5, s[6:7]
	v_cndmask_b32_e64 v3, v5, v3, s[6:7]
	v_cndmask_b32_e64 v5, v9, v11, s[6:7]
	ds_bpermute_b32 v6, v120, v6
	ds_bpermute_b32 v7, v120, v7
	ds_bpermute_b32 v13, v120, v5
	v_cndmask_b32_e64 v2, v4, v2, s[6:7]
	v_cndmask_b32_e64 v5, v11, v9, s[6:7]
	v_cndmask_b32_e64 v4, v10, v8, s[6:7]
	s_waitcnt lgkmcnt(1)
	v_pk_add_f32 v[2:3], v[2:3], v[6:7]
	s_waitcnt lgkmcnt(0)
	v_pk_add_f32 v[4:5], v[4:5], v[12:13]
	s_nop 0
	v_cndmask_b32_e64 v6, v2, v4, s[8:9]
	v_cndmask_b32_e64 v7, v3, v5, s[8:9]
	ds_bpermute_b32 v6, v121, v6
	ds_bpermute_b32 v7, v121, v7
	v_cndmask_b32_e64 v3, v5, v3, s[8:9]
	v_cndmask_b32_e64 v2, v4, v2, s[8:9]
	s_waitcnt lgkmcnt(0)
	v_pk_add_f32 v[2:3], v[2:3], v[6:7]
	s_cbranch_vccnz .LBB0_743
	ds_read2st64_b32 v[4:5], v124 offset1:1
	s_waitcnt lgkmcnt(0)
	v_pk_add_f32 v[2:3], v[2:3], v[4:5]
	s_branch .LBB0_743

.LBB0_1495:
	ds_read_b128 v[2:5], v123
	ds_read_b128 v[82:85], v123 offset:128
	s_waitcnt lgkmcnt(0)
	v_and_b32_e32 v6, 0xffff, v2
	v_lshrrev_b32_e32 v2, 16, v2
	v_mad_u32_u24 v18, v6, s25, v110
	v_mad_u32_u24 v2, v2, s25, v110
	global_load_dwordx2 v[10:11], v18, s[20:21] offset:16
	global_load_dwordx4 v[6:9], v18, s[20:21]
	global_load_dwordx2 v[16:17], v2, s[20:21] offset:16
	global_load_dwordx4 v[12:15], v2, s[20:21]
	v_and_b32_e32 v2, 0xffff, v3
	v_mad_u32_u24 v2, v2, s25, v110
	global_load_dwordx2 v[130:131], v2, s[20:21] offset:16
	global_load_dwordx4 v[126:129], v2, s[20:21]
	v_lshrrev_b32_e32 v2, 16, v3
	v_mad_u32_u24 v2, v2, s25, v110
	global_load_dwordx2 v[136:137], v2, s[20:21] offset:16
	global_load_dwordx4 v[132:135], v2, s[20:21]
	v_and_b32_e32 v2, 0xffff, v4
	v_mad_u32_u24 v2, v2, s25, v110
	global_load_dwordx2 v[142:143], v2, s[20:21] offset:16
	global_load_dwordx4 v[138:141], v2, s[20:21]
	v_lshrrev_b32_e32 v3, 16, v4
	v_and_b32_e32 v2, 0xffff, v5
	v_lshrrev_b32_e32 v4, 16, v5
	v_mad_u32_u24 v3, v3, s25, v110
	v_mad_u32_u24 v2, v2, s25, v110
	v_mad_u32_u24 v4, v4, s25, v110
	global_load_dwordx2 v[148:149], v3, s[20:21] offset:16
	global_load_dwordx4 v[144:147], v3, s[20:21]
	global_load_dwordx2 v[154:155], v2, s[20:21] offset:16
	global_load_dwordx4 v[150:153], v2, s[20:21]
	global_load_dwordx2 v[160:161], v4, s[20:21] offset:16
	global_load_dwordx4 v[156:159], v4, s[20:21]
	s_and_b64 vcc, exec, s[10:11]
	s_waitcnt vmcnt(14)
	v_cvt_scalef32_pk32_bf16_fp6 v[50:65], v[6:11], 1.0
	v_dot2_f32_bf16 v106, v50, v78, 0
	s_waitcnt vmcnt(12)
	v_cvt_scalef32_pk32_bf16_fp6 v[34:49], v[12:17], 1.0
	v_dot2_f32_bf16 v102, v34, v78, 0
	v_dot2_f32_bf16 v104, v35, v79, 0
	s_waitcnt vmcnt(10)
	v_cvt_scalef32_pk32_bf16_fp6 v[18:33], v[126:131], 1.0
	v_dot2_f32_bf16 v98, v18, v78, 0
	v_dot2_f32_bf16 v98, v20, v80, v98
	s_waitcnt vmcnt(8)
	v_cvt_scalef32_pk32_bf16_fp6 v[2:17], v[132:137], 1.0
	v_dot2_f32_bf16 v94, v2, v78, 0
	v_dot2_f32_bf16 v96, v3, v79, 0
	v_dot2_f32_bf16 v94, v4, v80, v94
	v_dot2_f32_bf16 v96, v5, v81, v96
	v_dot2_f32_bf16 v94, v6, v74, v94
	v_dot2_f32_bf16 v96, v7, v75, v96
	v_dot2_f32_bf16 v94, v8, v76, v94
	v_dot2_f32_bf16 v96, v9, v77, v96
	v_dot2_f32_bf16 v94, v10, v70, v94
	v_dot2_f32_bf16 v96, v11, v71, v96
	v_dot2_f32_bf16 v94, v12, v72, v94
	v_dot2_f32_bf16 v96, v13, v73, v96
	v_dot2_f32_bf16 v94, v14, v66, v94
	v_dot2_f32_bf16 v96, v15, v67, v96
	v_dot2_f32_bf16 v94, v16, v68, v94
	v_dot2_f32_bf16 v96, v17, v69, v96
	s_waitcnt vmcnt(6)
	v_cvt_scalef32_pk32_bf16_fp6 v[2:17], v[138:143], 1.0
	v_dot2_f32_bf16 v18, v2, v78, 0
	v_dot2_f32_bf16 v20, v3, v79, 0
	v_dot2_f32_bf16 v18, v4, v80, v18
	v_dot2_f32_bf16 v20, v5, v81, v20
	v_dot2_f32_bf16 v18, v6, v74, v18
	v_dot2_f32_bf16 v20, v7, v75, v20
	v_dot2_f32_bf16 v18, v8, v76, v18
	v_dot2_f32_bf16 v20, v9, v77, v20
	v_dot2_f32_bf16 v18, v10, v70, v18
	v_dot2_f32_bf16 v20, v11, v71, v20
	v_dot2_f32_bf16 v18, v12, v72, v18
	v_dot2_f32_bf16 v20, v13, v73, v20
	v_dot2_f32_bf16 v18, v14, v66, v18
	v_dot2_f32_bf16 v20, v15, v67, v20
	v_dot2_f32_bf16 v98, v22, v74, v98
	v_dot2_f32_bf16 v18, v16, v68, v18
	v_dot2_f32_bf16 v20, v17, v69, v20
	s_waitcnt vmcnt(4)
	v_cvt_scalef32_pk32_bf16_fp6 v[2:17], v[144:149], 1.0
	v_dot2_f32_bf16 v22, v2, v78, 0
	v_and_b32_e32 v2, 0xffff, v82
	v_dot2_f32_bf16 v102, v36, v80, v102
	v_dot2_f32_bf16 v104, v37, v81, v104
	v_mad_u32_u24 v2, v2, s25, v110
	v_dot2_f32_bf16 v102, v38, v74, v102
	v_dot2_f32_bf16 v104, v39, v75, v104
	global_load_dwordx2 v[38:39], v2, s[20:21] offset:16
	global_load_dwordx4 v[34:37], v2, s[20:21]
	v_dot2_f32_bf16 v98, v24, v76, v98
	v_dot2_f32_bf16 v100, v19, v79, 0
	v_dot2_f32_bf16 v102, v40, v76, v102
	v_dot2_f32_bf16 v104, v41, v77, v104
	v_dot2_f32_bf16 v24, v3, v79, 0
	v_lshrrev_b32_e32 v19, 16, v82
	v_dot2_f32_bf16 v102, v42, v70, v102
	v_dot2_f32_bf16 v104, v43, v71, v104
	v_dot2_f32_bf16 v22, v4, v80, v22
	v_dot2_f32_bf16 v24, v5, v81, v24
	v_mad_u32_u24 v19, v19, s25, v110
	v_dot2_f32_bf16 v102, v44, v72, v102
	v_dot2_f32_bf16 v104, v45, v73, v104
	v_dot2_f32_bf16 v22, v6, v74, v22
	v_dot2_f32_bf16 v24, v7, v75, v24
	global_load_dwordx2 v[44:45], v19, s[20:21] offset:16
	global_load_dwordx4 v[40:43], v19, s[20:21]
	v_dot2_f32_bf16 v22, v8, v76, v22
	v_dot2_f32_bf16 v24, v9, v77, v24
	v_dot2_f32_bf16 v22, v10, v70, v22
	v_dot2_f32_bf16 v24, v11, v71, v24
	v_dot2_f32_bf16 v22, v12, v72, v22
	v_dot2_f32_bf16 v24, v13, v73, v24
	v_dot2_f32_bf16 v98, v26, v70, v98
	v_dot2_f32_bf16 v22, v14, v66, v22
	v_dot2_f32_bf16 v24, v15, v67, v24
	v_dot2_f32_bf16 v98, v28, v72, v98
	v_dot2_f32_bf16 v22, v16, v68, v22
	v_dot2_f32_bf16 v24, v17, v69, v24
	s_waitcnt vmcnt(6)
	v_cvt_scalef32_pk32_bf16_fp6 v[2:17], v[150:155], 1.0
	v_dot2_f32_bf16 v26, v2, v78, 0
	v_dot2_f32_bf16 v28, v3, v79, 0
	v_and_b32_e32 v2, 0xffff, v83
	v_dot2_f32_bf16 v102, v46, v66, v102
	v_dot2_f32_bf16 v104, v47, v67, v104
	v_dot2_f32_bf16 v26, v4, v80, v26
	v_dot2_f32_bf16 v28, v5, v81, v28
	v_mad_u32_u24 v2, v2, s25, v110
	v_dot2_f32_bf16 v108, v51, v79, 0
	v_dot2_f32_bf16 v102, v48, v68, v102
	v_dot2_f32_bf16 v104, v49, v69, v104
	v_dot2_f32_bf16 v26, v6, v74, v26
	v_dot2_f32_bf16 v28, v7, v75, v28
	global_load_dwordx2 v[50:51], v2, s[20:21] offset:16
	global_load_dwordx4 v[46:49], v2, s[20:21]
	v_dot2_f32_bf16 v26, v8, v76, v26
	v_dot2_f32_bf16 v28, v9, v77, v28
	v_dot2_f32_bf16 v26, v10, v70, v26
	v_dot2_f32_bf16 v28, v11, v71, v28
	v_dot2_f32_bf16 v26, v12, v72, v26
	v_dot2_f32_bf16 v28, v13, v73, v28
	v_dot2_f32_bf16 v26, v14, v66, v26
	v_dot2_f32_bf16 v28, v15, v67, v28
	v_dot2_f32_bf16 v98, v30, v66, v98
	v_dot2_f32_bf16 v26, v16, v68, v26
	v_dot2_f32_bf16 v28, v17, v69, v28
	s_waitcnt vmcnt(6)
	v_cvt_scalef32_pk32_bf16_fp6 v[2:17], v[156:161], 1.0
	v_dot2_f32_bf16 v106, v52, v80, v106
	v_dot2_f32_bf16 v108, v53, v81, v108
	v_dot2_f32_bf16 v30, v2, v78, 0
	v_lshrrev_b32_e32 v2, 16, v83
	v_dot2_f32_bf16 v106, v54, v74, v106
	v_dot2_f32_bf16 v108, v55, v75, v108
	v_mad_u32_u24 v2, v2, s25, v110
	v_dot2_f32_bf16 v106, v56, v76, v106
	v_dot2_f32_bf16 v108, v57, v77, v108
	global_load_dwordx2 v[56:57], v2, s[20:21] offset:16
	global_load_dwordx4 v[52:55], v2, s[20:21]
	v_dot2_f32_bf16 v106, v58, v70, v106
	v_dot2_f32_bf16 v108, v59, v71, v108
	v_and_b32_e32 v2, 0xffff, v84
	v_dot2_f32_bf16 v106, v60, v72, v106
	v_dot2_f32_bf16 v108, v61, v73, v108
	v_mad_u32_u24 v2, v2, s25, v110
	v_dot2_f32_bf16 v106, v62, v66, v106
	v_dot2_f32_bf16 v108, v63, v67, v108
	global_load_dwordx2 v[62:63], v2, s[20:21] offset:16
	global_load_dwordx4 v[58:61], v2, s[20:21]
	v_lshrrev_b32_e32 v2, 16, v84
	v_mad_u32_u24 v2, v2, s25, v110
	global_load_dwordx2 v[130:131], v2, s[20:21] offset:16
	global_load_dwordx4 v[126:129], v2, s[20:21]
	v_and_b32_e32 v2, 0xffff, v85
	v_mad_u32_u24 v2, v2, s25, v110
	global_load_dwordx2 v[136:137], v2, s[20:21] offset:16
	global_load_dwordx4 v[132:135], v2, s[20:21]
	v_lshrrev_b32_e32 v2, 16, v85
	v_mad_u32_u24 v2, v2, s25, v110
	global_load_dwordx2 v[142:143], v2, s[20:21] offset:16
	global_load_dwordx4 v[138:141], v2, s[20:21]
	v_dot2_f32_bf16 v98, v32, v68, v98
	v_dot2_f32_bf16 v32, v3, v79, 0
	v_dot2_f32_bf16 v30, v4, v80, v30
	v_dot2_f32_bf16 v32, v5, v81, v32
	v_dot2_f32_bf16 v30, v6, v74, v30
	v_dot2_f32_bf16 v32, v7, v75, v32
	v_dot2_f32_bf16 v30, v8, v76, v30
	v_dot2_f32_bf16 v32, v9, v77, v32
	v_dot2_f32_bf16 v30, v10, v70, v30
	v_dot2_f32_bf16 v32, v11, v71, v32
	v_dot2_f32_bf16 v30, v12, v72, v30
	v_dot2_f32_bf16 v32, v13, v73, v32
	v_dot2_f32_bf16 v30, v14, v66, v30
	v_dot2_f32_bf16 v32, v15, v67, v32
	v_dot2_f32_bf16 v30, v16, v68, v30
	v_dot2_f32_bf16 v32, v17, v69, v32
	s_waitcnt vmcnt(14)
	v_cvt_scalef32_pk32_bf16_fp6 v[2:17], v[34:39], 1.0
	v_dot2_f32_bf16 v107, v2, v78, 0
	v_dot2_f32_bf16 v109, v3, v79, 0
	v_dot2_f32_bf16 v107, v4, v80, v107
	v_dot2_f32_bf16 v109, v5, v81, v109
	v_dot2_f32_bf16 v107, v6, v74, v107
	v_dot2_f32_bf16 v109, v7, v75, v109
	v_dot2_f32_bf16 v107, v8, v76, v107
	v_dot2_f32_bf16 v109, v9, v77, v109
	v_dot2_f32_bf16 v107, v10, v70, v107
	v_dot2_f32_bf16 v109, v11, v71, v109
	v_dot2_f32_bf16 v107, v12, v72, v107
	v_dot2_f32_bf16 v109, v13, v73, v109
	v_dot2_f32_bf16 v107, v14, v66, v107
	v_dot2_f32_bf16 v109, v15, v67, v109
	v_dot2_f32_bf16 v107, v16, v68, v107
	v_dot2_f32_bf16 v109, v17, v69, v109
	s_waitcnt vmcnt(12)
	v_cvt_scalef32_pk32_bf16_fp6 v[2:17], v[40:45], 1.0
	v_dot2_f32_bf16 v103, v2, v78, 0
	v_dot2_f32_bf16 v105, v3, v79, 0
	v_dot2_f32_bf16 v103, v4, v80, v103
	v_dot2_f32_bf16 v105, v5, v81, v105
	v_dot2_f32_bf16 v103, v6, v74, v103
	v_dot2_f32_bf16 v105, v7, v75, v105
	v_dot2_f32_bf16 v103, v8, v76, v103
	v_dot2_f32_bf16 v105, v9, v77, v105
	v_dot2_f32_bf16 v103, v10, v70, v103
	v_dot2_f32_bf16 v105, v11, v71, v105
	v_dot2_f32_bf16 v103, v12, v72, v103
	v_dot2_f32_bf16 v105, v13, v73, v105
	v_dot2_f32_bf16 v103, v14, v66, v103
	v_dot2_f32_bf16 v105, v15, v67, v105
	v_dot2_f32_bf16 v103, v16, v68, v103
	v_dot2_f32_bf16 v105, v17, v69, v105
	s_waitcnt vmcnt(10)
	v_cvt_scalef32_pk32_bf16_fp6 v[2:17], v[46:51], 1.0
	v_dot2_f32_bf16 v99, v2, v78, 0
	v_dot2_f32_bf16 v101, v3, v79, 0
	v_dot2_f32_bf16 v99, v4, v80, v99
	v_dot2_f32_bf16 v101, v5, v81, v101
	v_dot2_f32_bf16 v99, v6, v74, v99
	v_dot2_f32_bf16 v101, v7, v75, v101
	v_dot2_f32_bf16 v99, v8, v76, v99
	v_dot2_f32_bf16 v101, v9, v77, v101
	v_dot2_f32_bf16 v99, v10, v70, v99
	v_dot2_f32_bf16 v101, v11, v71, v101
	v_dot2_f32_bf16 v99, v12, v72, v99
	v_dot2_f32_bf16 v101, v13, v73, v101
	v_dot2_f32_bf16 v99, v14, v66, v99
	v_dot2_f32_bf16 v101, v15, v67, v101
	v_dot2_f32_bf16 v99, v16, v68, v99
	v_dot2_f32_bf16 v101, v17, v69, v101
	s_waitcnt vmcnt(8)
	v_cvt_scalef32_pk32_bf16_fp6 v[2:17], v[52:57], 1.0
	v_dot2_f32_bf16 v95, v2, v78, 0
	v_dot2_f32_bf16 v97, v3, v79, 0
	v_dot2_f32_bf16 v95, v4, v80, v95
	v_dot2_f32_bf16 v97, v5, v81, v97
	v_dot2_f32_bf16 v95, v6, v74, v95
	v_dot2_f32_bf16 v97, v7, v75, v97
	v_dot2_f32_bf16 v95, v8, v76, v95
	v_dot2_f32_bf16 v97, v9, v77, v97
	v_dot2_f32_bf16 v95, v10, v70, v95
	v_dot2_f32_bf16 v97, v11, v71, v97
	v_dot2_f32_bf16 v95, v12, v72, v95
	v_dot2_f32_bf16 v97, v13, v73, v97
	v_dot2_f32_bf16 v95, v14, v66, v95
	v_dot2_f32_bf16 v97, v15, v67, v97
	v_dot2_f32_bf16 v100, v21, v81, v100
	v_dot2_f32_bf16 v95, v16, v68, v95
	v_dot2_f32_bf16 v97, v17, v69, v97
	s_waitcnt vmcnt(6)
	v_cvt_scalef32_pk32_bf16_fp6 v[2:17], v[58:63], 1.0
	v_dot2_f32_bf16 v19, v2, v78, 0
	v_dot2_f32_bf16 v21, v3, v79, 0
	v_dot2_f32_bf16 v19, v4, v80, v19
	v_dot2_f32_bf16 v21, v5, v81, v21
	v_dot2_f32_bf16 v19, v6, v74, v19
	v_dot2_f32_bf16 v21, v7, v75, v21
	v_dot2_f32_bf16 v19, v8, v76, v19
	v_dot2_f32_bf16 v21, v9, v77, v21
	v_dot2_f32_bf16 v19, v10, v70, v19
	v_dot2_f32_bf16 v21, v11, v71, v21
	v_dot2_f32_bf16 v19, v12, v72, v19
	v_dot2_f32_bf16 v21, v13, v73, v21
	v_dot2_f32_bf16 v100, v23, v75, v100
	v_dot2_f32_bf16 v19, v14, v66, v19
	v_dot2_f32_bf16 v21, v15, v67, v21
	v_dot2_f32_bf16 v100, v25, v77, v100
	v_dot2_f32_bf16 v19, v16, v68, v19
	v_dot2_f32_bf16 v21, v17, v69, v21
	s_waitcnt vmcnt(4)
	v_cvt_scalef32_pk32_bf16_fp6 v[2:17], v[126:131], 1.0
	v_dot2_f32_bf16 v23, v2, v78, 0
	v_dot2_f32_bf16 v25, v3, v79, 0
	v_dot2_f32_bf16 v23, v4, v80, v23
	v_dot2_f32_bf16 v25, v5, v81, v25
	v_dot2_f32_bf16 v23, v6, v74, v23
	v_dot2_f32_bf16 v25, v7, v75, v25
	v_dot2_f32_bf16 v23, v8, v76, v23
	v_dot2_f32_bf16 v25, v9, v77, v25
	v_dot2_f32_bf16 v23, v10, v70, v23
	v_dot2_f32_bf16 v25, v11, v71, v25
	v_dot2_f32_bf16 v23, v12, v72, v23
	v_dot2_f32_bf16 v25, v13, v73, v25
	v_dot2_f32_bf16 v100, v27, v71, v100
	v_dot2_f32_bf16 v23, v14, v66, v23
	v_dot2_f32_bf16 v25, v15, v67, v25
	v_dot2_f32_bf16 v100, v29, v73, v100
	v_dot2_f32_bf16 v23, v16, v68, v23
	v_dot2_f32_bf16 v25, v17, v69, v25
	s_waitcnt vmcnt(2)
	v_cvt_scalef32_pk32_bf16_fp6 v[2:17], v[132:137], 1.0
	v_dot2_f32_bf16 v27, v2, v78, 0
	v_dot2_f32_bf16 v29, v3, v79, 0
	v_dot2_f32_bf16 v27, v4, v80, v27
	v_dot2_f32_bf16 v29, v5, v81, v29
	v_dot2_f32_bf16 v27, v6, v74, v27
	v_dot2_f32_bf16 v29, v7, v75, v29
	v_dot2_f32_bf16 v27, v8, v76, v27
	v_dot2_f32_bf16 v29, v9, v77, v29
	v_dot2_f32_bf16 v27, v10, v70, v27
	v_dot2_f32_bf16 v29, v11, v71, v29
	v_dot2_f32_bf16 v27, v12, v72, v27
	v_dot2_f32_bf16 v29, v13, v73, v29
	v_dot2_f32_bf16 v100, v31, v67, v100
	v_dot2_f32_bf16 v27, v14, v66, v27
	v_dot2_f32_bf16 v29, v15, v67, v29
	v_dot2_f32_bf16 v100, v33, v69, v100
	v_dot2_f32_bf16 v27, v16, v68, v27
	v_dot2_f32_bf16 v29, v17, v69, v29
	s_waitcnt vmcnt(0)
	v_cvt_scalef32_pk32_bf16_fp6 v[2:17], v[138:143], 1.0
	v_dot2_f32_bf16 v31, v2, v78, 0
	v_dot2_f32_bf16 v33, v3, v79, 0
	v_dot2_f32_bf16 v31, v4, v80, v31
	v_dot2_f32_bf16 v33, v5, v81, v33
	v_dot2_f32_bf16 v31, v6, v74, v31
	v_dot2_f32_bf16 v33, v7, v75, v33
	v_dot2_f32_bf16 v31, v8, v76, v31
	v_dot2_f32_bf16 v33, v9, v77, v33
	v_dot2_f32_bf16 v31, v10, v70, v31
	v_dot2_f32_bf16 v33, v11, v71, v33
	v_dot2_f32_bf16 v31, v12, v72, v31
	v_dot2_f32_bf16 v33, v13, v73, v33
	v_dot2_f32_bf16 v31, v14, v66, v31
	v_dot2_f32_bf16 v33, v15, v67, v33
	v_pk_add_f32 v[8:9], v[104:105], v[102:103]
	v_pk_add_f32 v[10:11], v[24:25], v[22:23]
	v_dot2_f32_bf16 v31, v16, v68, v31
	v_dot2_f32_bf16 v33, v17, v69, v33
	v_cndmask_b32_e64 v7, v8, v10, s[2:3]
	v_pk_add_f32 v[14:15], v[100:101], v[98:99]
	v_pk_add_f32 v[16:17], v[28:29], v[26:27]
	v_dot2_f32_bf16 v106, v64, v68, v106
	v_dot2_f32_bf16 v108, v65, v69, v108
	v_pk_add_f32 v[4:5], v[20:21], v[18:19]
	ds_bpermute_b32 v12, v119, v7
	v_cndmask_b32_e64 v7, v14, v16, s[2:3]
	v_pk_add_f32 v[20:21], v[96:97], v[94:95]
	v_pk_add_f32 v[22:23], v[32:33], v[30:31]
	v_pk_add_f32 v[2:3], v[108:109], v[106:107]
	ds_bpermute_b32 v18, v119, v7
	v_cndmask_b32_e64 v7, v20, v22, s[2:3]
	v_cndmask_b32_e64 v6, v2, v4, s[2:3]
	ds_bpermute_b32 v24, v119, v7
	v_cndmask_b32_e64 v7, v3, v5, s[2:3]
	ds_bpermute_b32 v6, v119, v6
	ds_bpermute_b32 v7, v119, v7
	v_cndmask_b32_e64 v3, v5, v3, s[2:3]
	v_cndmask_b32_e64 v2, v4, v2, s[2:3]
	v_cndmask_b32_e64 v5, v15, v17, s[2:3]
	ds_bpermute_b32 v19, v119, v5
	s_waitcnt lgkmcnt(1)
	v_pk_add_f32 v[2:3], v[2:3], v[6:7]
	v_cndmask_b32_e64 v7, v9, v11, s[2:3]
	ds_bpermute_b32 v13, v119, v7
	v_cndmask_b32_e64 v7, v21, v23, s[2:3]
	ds_bpermute_b32 v25, v119, v7
	v_cndmask_b32_e64 v9, v11, v9, s[2:3]
	v_cndmask_b32_e64 v8, v10, v8, s[2:3]
	v_cndmask_b32_e64 v11, v23, v21, s[2:3]
	v_cndmask_b32_e64 v10, v22, v20, s[2:3]
	v_cndmask_b32_e64 v5, v17, v15, s[2:3]
	v_cndmask_b32_e64 v4, v16, v14, s[2:3]
	s_waitcnt lgkmcnt(1)
	v_pk_add_f32 v[8:9], v[8:9], v[12:13]
	s_waitcnt lgkmcnt(0)
	v_pk_add_f32 v[10:11], v[10:11], v[24:25]
	v_pk_add_f32 v[4:5], v[4:5], v[18:19]
	v_cndmask_b32_e64 v7, v8, v10, s[4:5]
	v_cndmask_b32_e64 v6, v2, v4, s[4:5]
	ds_bpermute_b32 v12, v120, v7
	v_cndmask_b32_e64 v7, v3, v5, s[4:5]
	v_cndmask_b32_e64 v3, v5, v3, s[4:5]
	v_cndmask_b32_e64 v5, v9, v11, s[4:5]
	ds_bpermute_b32 v6, v120, v6
	ds_bpermute_b32 v7, v120, v7
	ds_bpermute_b32 v13, v120, v5
	v_cndmask_b32_e64 v2, v4, v2, s[4:5]
	v_cndmask_b32_e64 v5, v11, v9, s[4:5]
	v_cndmask_b32_e64 v4, v10, v8, s[4:5]
	s_waitcnt lgkmcnt(1)
	v_pk_add_f32 v[2:3], v[2:3], v[6:7]
	s_waitcnt lgkmcnt(0)
	v_pk_add_f32 v[4:5], v[4:5], v[12:13]
	s_nop 0
	v_cndmask_b32_e64 v6, v2, v4, s[6:7]
	v_cndmask_b32_e64 v7, v3, v5, s[6:7]
	ds_bpermute_b32 v6, v121, v6
	ds_bpermute_b32 v7, v121, v7
	v_cndmask_b32_e64 v3, v5, v3, s[6:7]
	v_cndmask_b32_e64 v2, v4, v2, s[6:7]
	s_waitcnt lgkmcnt(0)
	v_pk_add_f32 v[2:3], v[2:3], v[6:7]
	s_cbranch_vccnz .LBB0_1492
	ds_read2st64_b32 v[4:5], v124 offset1:1
	s_waitcnt lgkmcnt(0)
	v_pk_add_f32 v[2:3], v[2:3], v[4:5]
	s_branch .LBB0_1492
